# speedup vs baseline: 1.0016x; 1.0016x over previous
.LBB0_60:
	s_andn2_b64 vcc, exec, s[4:5]
	s_cbranch_vccnz .LBB0_98
	s_sleep 24
	s_load_dwordx2 s[4:5], s[0:1], 0x0
	s_lshl_b32 s3, s2, 12
	v_mov_b32_e32 v2, 0
	v_or_b32_e32 v6, s3, v0
	s_mov_b32 s10, 0xf4240
	s_waitcnt lgkmcnt(0)
	s_add_u32 s6, s4, 0x3d0900
	v_lshlrev_b32_e32 v1, 2, v0
	s_addc_u32 s7, s5, 0
	v_cmp_gt_i32_e32 vcc, s10, v6
	v_mov_b32_e32 v3, v2
	v_mov_b32_e32 v4, v2
	v_mov_b32_e32 v5, v2
	v_mov_b32_e32 v11, -1
	v_mov_b32_e32 v10, -1
	ds_write_b32 v1, v2 offset:16384
	s_waitcnt lgkmcnt(0)
	s_barrier
	s_and_saveexec_b64 s[8:9], vcc
	s_cbranch_execz .LBB0_63
	v_ashrrev_i32_e32 v7, 31, v6
	v_lshlrev_b64 v[4:5], 2, v[6:7]
	v_lshl_add_u64 v[8:9], s[6:7], 0, v[4:5]
	global_load_dword v8, v[8:9], off nt
	v_lshl_add_u64 v[4:5], s[4:5], 0, v[4:5]
	global_load_dword v3, v[4:5], off nt
	s_mov_b32 s11, 0x5397829d
	s_movk_i32 s12, 0x7f9e
	v_mov_b32_e32 v13, v2
	v_mov_b32_e32 v14, v2
	v_mov_b32_e32 v15, v2
	s_waitcnt vmcnt(1)
	v_mul_hi_i32 v4, v8, s11
	v_lshrrev_b32_e32 v5, 31, v4
	v_ashrrev_i32_e32 v4, 5, v4
	v_add_u32_e32 v10, v4, v5
	v_mad_u64_u32 v[4:5], s[12:13], v10, s12, v[8:9]
	s_waitcnt vmcnt(0)
	v_lshl_or_b32 v12, v4, 17, v3
	v_mov_b64_e32 v[2:3], v[12:13]
	v_mov_b64_e32 v[4:5], v[14:15]
